# GEMM K-loops: closing s_barrier issued right after the last MFMA (bookkeeping moved behind it), s_setprio 1 hoisted before the opening barrier, doubled lgkmcnt wait emitted once
# speedup vs baseline: 1.1547x; 1.0106x over previous
.LBB0_267:
	s_add_u32 s16, s14, 0x80
	s_addc_u32 s17, s15, 0
	s_add_i32 s41, 0, 0x10000
	v_add_u32_e32 v144, s41, v147
	ds_read_b128 v[150:153], v144
	ds_read_b128 v[154:157], v144 offset:1024
	ds_read_b128 v[158:161], v144 offset:2048
	ds_read_b128 v[162:165], v144 offset:3072
	s_cmp_eq_u32 s40, 28
	s_cselect_b32 s19, s11, s17
	s_cselect_b32 s18, s10, s16
	s_cselect_b32 s17, s13, s39
	s_cselect_b32 s16, s12, s38
	v_lshl_add_u64 v[144:145], s[14:15], 0, v[142:143]
	s_add_i32 m0, s27, 0xc000
	ds_read_b128 v[172:175], v148
	ds_read_b128 v[176:179], v148 offset:1024
	ds_read_b128 v[180:183], v148 offset:2048
	ds_read_b128 v[208:211], v148 offset:3072
	ds_read_b128 v[212:215], v148 offset:4096
	ds_read_b128 v[216:219], v148 offset:5120
	ds_read_b128 v[220:223], v148 offset:6144
	ds_read_b128 v[224:227], v148 offset:7168
	global_load_lds_dwordx4 v[144:145], off
	v_lshl_add_u64 v[144:145], s[14:15], 0, v[140:141]
	s_add_i32 m0, s27, 0xe000
	s_nop 0
	global_load_lds_dwordx4 v[144:145], off
	s_waitcnt lgkmcnt(8)
	s_setprio 1
	s_barrier
	s_waitcnt lgkmcnt(0)
	v_mfma_f32_16x16x32_bf16 v[124:127], v[150:153], v[172:175], v[124:127]
	v_mfma_f32_16x16x32_bf16 v[120:123], v[158:161], v[172:175], v[120:123]
	v_mfma_f32_16x16x32_bf16 v[116:119], v[150:153], v[180:183], v[116:119]
	v_mfma_f32_16x16x32_bf16 v[108:111], v[158:161], v[180:183], v[108:111]
	v_mfma_f32_16x16x32_bf16 v[100:103], v[150:153], v[212:215], v[100:103]
	v_mfma_f32_16x16x32_bf16 v[92:95], v[158:161], v[212:215], v[92:95]
	v_mfma_f32_16x16x32_bf16 v[84:87], v[150:153], v[220:223], v[84:87]
	v_mfma_f32_16x16x32_bf16 v[76:79], v[158:161], v[220:223], v[76:79]
	v_mfma_f32_16x16x32_bf16 v[124:127], v[154:157], v[176:179], v[124:127]
	v_mfma_f32_16x16x32_bf16 v[120:123], v[162:165], v[176:179], v[120:123]
	v_mfma_f32_16x16x32_bf16 v[116:119], v[154:157], v[208:211], v[116:119]
	v_mfma_f32_16x16x32_bf16 v[108:111], v[162:165], v[208:211], v[108:111]
	v_mfma_f32_16x16x32_bf16 v[100:103], v[154:157], v[216:219], v[100:103]
	v_mfma_f32_16x16x32_bf16 v[92:95], v[162:165], v[216:219], v[92:95]
	v_mfma_f32_16x16x32_bf16 v[84:87], v[154:157], v[224:227], v[84:87]
	v_mfma_f32_16x16x32_bf16 v[76:79], v[162:165], v[224:227], v[76:79]
	s_barrier
	s_setprio 0
	s_add_i32 s44, 0, 0x14000
	v_add_u32_e32 v144, s44, v147
	s_add_i32 s41, s41, s25
	ds_read_b128 v[228:231], v144
	ds_read_b128 v[232:235], v144 offset:1024
	ds_read_b128 v[236:239], v144 offset:2048
	ds_read_b128 v[240:243], v144 offset:3072
	v_lshl_add_u64 v[144:145], s[16:17], 0, v[138:139]
	s_mov_b32 m0, s41
	v_lshl_add_u64 v[166:167], s[16:17], 0, v[132:133]
	global_load_lds_dwordx4 v[144:145], off
	s_add_i32 m0, s41, 0x2000
	s_nop 0
	global_load_lds_dwordx4 v[166:167], off
	s_setprio 1
	s_barrier
	s_waitcnt lgkmcnt(0)
	v_mfma_f32_16x16x32_bf16 v[112:115], v[228:231], v[172:175], v[112:115]
	v_mfma_f32_16x16x32_bf16 v[104:107], v[236:239], v[172:175], v[104:107]
	v_mfma_f32_16x16x32_bf16 v[96:99], v[228:231], v[180:183], v[96:99]
	v_mfma_f32_16x16x32_bf16 v[88:91], v[236:239], v[180:183], v[88:91]
	v_mfma_f32_16x16x32_bf16 v[80:83], v[228:231], v[212:215], v[80:83]
	v_mfma_f32_16x16x32_bf16 v[72:75], v[236:239], v[212:215], v[72:75]
	v_mfma_f32_16x16x32_bf16 v[68:71], v[228:231], v[220:223], v[68:71]
	v_mfma_f32_16x16x32_bf16 v[64:67], v[236:239], v[220:223], v[64:67]
	v_mfma_f32_16x16x32_bf16 v[112:115], v[232:235], v[176:179], v[112:115]
	v_mfma_f32_16x16x32_bf16 v[104:107], v[240:243], v[176:179], v[104:107]
	v_mfma_f32_16x16x32_bf16 v[96:99], v[232:235], v[208:211], v[96:99]
	v_mfma_f32_16x16x32_bf16 v[88:91], v[240:243], v[208:211], v[88:91]
	v_mfma_f32_16x16x32_bf16 v[80:83], v[232:235], v[216:219], v[80:83]
	v_mfma_f32_16x16x32_bf16 v[72:75], v[240:243], v[216:219], v[72:75]
	v_mfma_f32_16x16x32_bf16 v[68:71], v[232:235], v[224:227], v[68:71]
	v_mfma_f32_16x16x32_bf16 v[64:67], v[240:243], v[224:227], v[64:67]
	s_barrier
	s_setprio 0
	s_mov_b32 m0, s27
	v_lshl_add_u64 v[184:185], s[18:19], 0, v[134:135]
	ds_read_b128 v[172:175], v148 offset:16384
	ds_read_b128 v[176:179], v148 offset:17408
	ds_read_b128 v[180:183], v148 offset:18432
	ds_read_b128 v[208:211], v148 offset:19456
	ds_read_b128 v[212:215], v148 offset:20480
	ds_read_b128 v[216:219], v148 offset:21504
	ds_read_b128 v[220:223], v148 offset:22528
	ds_read_b128 v[224:227], v148 offset:23552
	global_load_lds_dwordx4 v[184:185], off
	v_lshl_add_u64 v[244:245], s[18:19], 0, v[128:129]
	s_mov_b32 m0, s28
	s_nop 0
	global_load_lds_dwordx4 v[244:245], off
	s_setprio 1
	s_barrier
	s_waitcnt lgkmcnt(0)
	v_mfma_f32_16x16x32_bf16 v[60:63], v[150:153], v[172:175], v[60:63]
	v_mfma_f32_16x16x32_bf16 v[56:59], v[158:161], v[172:175], v[56:59]
	v_mfma_f32_16x16x32_bf16 v[44:47], v[150:153], v[180:183], v[44:47]
	v_mfma_f32_16x16x32_bf16 v[36:39], v[158:161], v[180:183], v[36:39]
	v_mfma_f32_16x16x32_bf16 v[20:23], v[150:153], v[212:215], v[20:23]
	v_mfma_f32_16x16x32_bf16 v[12:15], v[158:161], v[212:215], v[12:15]
	v_mfma_f32_16x16x32_bf16 v[4:7], v[150:153], v[220:223], v[4:7]
	v_mfma_f32_16x16x32_bf16 v[0:3], v[158:161], v[220:223], v[0:3]
	v_mfma_f32_16x16x32_bf16 v[60:63], v[154:157], v[176:179], v[60:63]
	v_mfma_f32_16x16x32_bf16 v[56:59], v[162:165], v[176:179], v[56:59]
	v_mfma_f32_16x16x32_bf16 v[44:47], v[154:157], v[208:211], v[44:47]
	v_mfma_f32_16x16x32_bf16 v[36:39], v[162:165], v[208:211], v[36:39]
	v_mfma_f32_16x16x32_bf16 v[20:23], v[154:157], v[216:219], v[20:23]
	v_mfma_f32_16x16x32_bf16 v[12:15], v[162:165], v[216:219], v[12:15]
	v_mfma_f32_16x16x32_bf16 v[4:7], v[154:157], v[224:227], v[4:7]
	v_mfma_f32_16x16x32_bf16 v[0:3], v[162:165], v[224:227], v[0:3]
	s_barrier
	s_setprio 0
	s_add_u32 s42, s16, 0x80000
	s_addc_u32 s43, s17, 0
	s_add_i32 s41, s44, s25
	v_lshl_add_u64 v[150:151], s[42:43], 0, v[138:139]
	s_mov_b32 m0, s41
	s_nop 0
	global_load_lds_dwordx4 v[150:151], off
	v_lshl_add_u64 v[150:151], s[42:43], 0, v[132:133]
	s_add_i32 m0, s41, 0x2000
	s_nop 0
	global_load_lds_dwordx4 v[150:151], off
	s_waitcnt vmcnt(6)
	s_setprio 1
	s_barrier
	v_mfma_f32_16x16x32_bf16 v[40:43], v[228:231], v[172:175], v[40:43]
	v_mfma_f32_16x16x32_bf16 v[28:31], v[236:239], v[172:175], v[28:31]
	v_mfma_f32_16x16x32_bf16 v[16:19], v[228:231], v[180:183], v[16:19]
	v_mfma_f32_16x16x32_bf16 v[8:11], v[236:239], v[180:183], v[8:11]
	v_mfma_f32_16x16x32_bf16 v[52:55], v[228:231], v[212:215], v[52:55]
	v_mfma_f32_16x16x32_bf16 v[48:51], v[236:239], v[212:215], v[48:51]
	v_mfma_f32_16x16x32_bf16 v[32:35], v[228:231], v[220:223], v[32:35]
	v_mfma_f32_16x16x32_bf16 v[24:27], v[236:239], v[220:223], v[24:27]
	v_mfma_f32_16x16x32_bf16 v[40:43], v[232:235], v[176:179], v[40:43]
	v_mfma_f32_16x16x32_bf16 v[28:31], v[240:243], v[176:179], v[28:31]
	v_mfma_f32_16x16x32_bf16 v[16:19], v[232:235], v[208:211], v[16:19]
	v_mfma_f32_16x16x32_bf16 v[8:11], v[240:243], v[208:211], v[8:11]
	v_mfma_f32_16x16x32_bf16 v[52:55], v[232:235], v[216:219], v[52:55]
	v_mfma_f32_16x16x32_bf16 v[48:51], v[240:243], v[216:219], v[48:51]
	v_mfma_f32_16x16x32_bf16 v[32:35], v[232:235], v[224:227], v[32:35]
	v_mfma_f32_16x16x32_bf16 v[24:27], v[240:243], v[224:227], v[24:27]
	s_barrier
	s_setprio 0
	s_add_i32 s41, 0, 0x18000
	v_add_u32_e32 v149, s41, v147
	ds_read_b128 v[150:153], v149
	ds_read_b128 v[154:157], v149 offset:1024
	ds_read_b128 v[158:161], v149 offset:2048
	ds_read_b128 v[162:165], v149 offset:3072
	s_mov_b32 m0, s29
	v_lshl_add_u64 v[228:229], s[18:19], 0, v[136:137]
	ds_read_b128 v[172:175], v148 offset:32768
	ds_read_b128 v[176:179], v148 offset:33792
	ds_read_b128 v[180:183], v148 offset:34816
	ds_read_b128 v[208:211], v148 offset:35840
	ds_read_b128 v[212:215], v148 offset:36864
	ds_read_b128 v[216:219], v148 offset:37888
	ds_read_b128 v[220:223], v148 offset:38912
	ds_read_b128 v[224:227], v148 offset:39936
	global_load_lds_dwordx4 v[228:229], off
	v_lshl_add_u64 v[228:229], s[18:19], 0, v[130:131]
	s_mov_b32 m0, s30
	s_nop 0
	global_load_lds_dwordx4 v[228:229], off
	s_waitcnt lgkmcnt(8)
	s_setprio 1
	s_barrier
	s_waitcnt lgkmcnt(0)
	v_mfma_f32_16x16x32_bf16 v[124:127], v[150:153], v[172:175], v[124:127]
	v_mfma_f32_16x16x32_bf16 v[120:123], v[158:161], v[172:175], v[120:123]
	v_mfma_f32_16x16x32_bf16 v[116:119], v[150:153], v[180:183], v[116:119]
	v_mfma_f32_16x16x32_bf16 v[108:111], v[158:161], v[180:183], v[108:111]
	v_mfma_f32_16x16x32_bf16 v[100:103], v[150:153], v[212:215], v[100:103]
	v_mfma_f32_16x16x32_bf16 v[92:95], v[158:161], v[212:215], v[92:95]
	v_mfma_f32_16x16x32_bf16 v[84:87], v[150:153], v[220:223], v[84:87]
	v_mfma_f32_16x16x32_bf16 v[76:79], v[158:161], v[220:223], v[76:79]
	v_mfma_f32_16x16x32_bf16 v[124:127], v[154:157], v[176:179], v[124:127]
	v_mfma_f32_16x16x32_bf16 v[120:123], v[162:165], v[176:179], v[120:123]
	v_mfma_f32_16x16x32_bf16 v[116:119], v[154:157], v[208:211], v[116:119]
	v_mfma_f32_16x16x32_bf16 v[108:111], v[162:165], v[208:211], v[108:111]
	v_mfma_f32_16x16x32_bf16 v[100:103], v[154:157], v[216:219], v[100:103]
	v_mfma_f32_16x16x32_bf16 v[92:95], v[162:165], v[216:219], v[92:95]
	v_mfma_f32_16x16x32_bf16 v[84:87], v[154:157], v[224:227], v[84:87]
	v_mfma_f32_16x16x32_bf16 v[76:79], v[162:165], v[224:227], v[76:79]
	s_barrier
	s_setprio 0
	s_add_i32 s18, 0, 0x1c000
	s_add_i32 s19, s41, s25
	v_add_u32_e32 v149, s18, v147
	v_lshl_add_u64 v[144:145], v[144:145], 0, s[94:95]
	s_mov_b32 m0, s19
	ds_read_b128 v[228:231], v149
	ds_read_b128 v[232:235], v149 offset:1024
	ds_read_b128 v[236:239], v149 offset:2048
	ds_read_b128 v[240:243], v149 offset:3072
	global_load_lds_dwordx4 v[144:145], off
	v_lshl_add_u64 v[144:145], v[166:167], 0, s[94:95]
	s_add_i32 m0, s19, 0x2000
	s_nop 0
	global_load_lds_dwordx4 v[144:145], off
	s_setprio 1
	s_barrier
	s_waitcnt lgkmcnt(0)
	v_mfma_f32_16x16x32_bf16 v[112:115], v[228:231], v[172:175], v[112:115]
	v_mfma_f32_16x16x32_bf16 v[104:107], v[236:239], v[172:175], v[104:107]
	v_mfma_f32_16x16x32_bf16 v[96:99], v[228:231], v[180:183], v[96:99]
	v_mfma_f32_16x16x32_bf16 v[88:91], v[236:239], v[180:183], v[88:91]
	v_mfma_f32_16x16x32_bf16 v[80:83], v[228:231], v[212:215], v[80:83]
	v_mfma_f32_16x16x32_bf16 v[72:75], v[236:239], v[212:215], v[72:75]
	v_mfma_f32_16x16x32_bf16 v[68:71], v[228:231], v[220:223], v[68:71]
	v_mfma_f32_16x16x32_bf16 v[64:67], v[236:239], v[220:223], v[64:67]
	v_mfma_f32_16x16x32_bf16 v[112:115], v[232:235], v[176:179], v[112:115]
	v_mfma_f32_16x16x32_bf16 v[104:107], v[240:243], v[176:179], v[104:107]
	v_mfma_f32_16x16x32_bf16 v[96:99], v[232:235], v[208:211], v[96:99]
	v_mfma_f32_16x16x32_bf16 v[88:91], v[240:243], v[208:211], v[88:91]
	v_mfma_f32_16x16x32_bf16 v[80:83], v[232:235], v[216:219], v[80:83]
	v_mfma_f32_16x16x32_bf16 v[72:75], v[240:243], v[216:219], v[72:75]
	v_mfma_f32_16x16x32_bf16 v[68:71], v[232:235], v[224:227], v[68:71]
	v_mfma_f32_16x16x32_bf16 v[64:67], v[240:243], v[224:227], v[64:67]
	s_barrier
	s_setprio 0
	s_mov_b32 m0, s31
	v_lshl_add_u64 v[144:145], v[184:185], 0, s[94:95]
	ds_read_b128 v[172:175], v148 offset:49152
	ds_read_b128 v[176:179], v148 offset:50176
	ds_read_b128 v[180:183], v148 offset:51200
	ds_read_b128 v[208:211], v148 offset:52224
	ds_read_b128 v[212:215], v148 offset:53248
	ds_read_b128 v[216:219], v148 offset:54272
	ds_read_b128 v[220:223], v148 offset:55296
	ds_read_b128 v[224:227], v148 offset:56320
	global_load_lds_dwordx4 v[144:145], off
	v_lshl_add_u64 v[144:145], v[244:245], 0, s[94:95]
	s_mov_b32 m0, s34
	s_nop 0
	global_load_lds_dwordx4 v[144:145], off
	s_setprio 1
	s_barrier
	s_waitcnt lgkmcnt(0)
	v_mfma_f32_16x16x32_bf16 v[60:63], v[150:153], v[172:175], v[60:63]
	v_mfma_f32_16x16x32_bf16 v[56:59], v[158:161], v[172:175], v[56:59]
	v_mfma_f32_16x16x32_bf16 v[44:47], v[150:153], v[180:183], v[44:47]
	v_mfma_f32_16x16x32_bf16 v[36:39], v[158:161], v[180:183], v[36:39]
	v_mfma_f32_16x16x32_bf16 v[20:23], v[150:153], v[212:215], v[20:23]
	v_mfma_f32_16x16x32_bf16 v[12:15], v[158:161], v[212:215], v[12:15]
	v_mfma_f32_16x16x32_bf16 v[4:7], v[150:153], v[220:223], v[4:7]
	v_mfma_f32_16x16x32_bf16 v[0:3], v[158:161], v[220:223], v[0:3]
	v_mfma_f32_16x16x32_bf16 v[60:63], v[154:157], v[176:179], v[60:63]
	v_mfma_f32_16x16x32_bf16 v[56:59], v[162:165], v[176:179], v[56:59]
	v_mfma_f32_16x16x32_bf16 v[44:47], v[154:157], v[208:211], v[44:47]
	v_mfma_f32_16x16x32_bf16 v[36:39], v[162:165], v[208:211], v[36:39]
	v_mfma_f32_16x16x32_bf16 v[20:23], v[154:157], v[216:219], v[20:23]
	v_mfma_f32_16x16x32_bf16 v[12:15], v[162:165], v[216:219], v[12:15]
	v_mfma_f32_16x16x32_bf16 v[4:7], v[154:157], v[224:227], v[4:7]
	v_mfma_f32_16x16x32_bf16 v[0:3], v[162:165], v[224:227], v[0:3]
	s_barrier
	s_setprio 0
	s_add_u32 s16, s16, 0x80080
	s_addc_u32 s17, s17, 0
	s_add_i32 s18, s18, s25
	v_lshl_add_u64 v[144:145], s[16:17], 0, v[138:139]
	s_mov_b32 m0, s18
	s_nop 0
	global_load_lds_dwordx4 v[144:145], off
	v_lshl_add_u64 v[144:145], s[16:17], 0, v[132:133]
	s_add_i32 m0, s18, 0x2000
	s_nop 0
	global_load_lds_dwordx4 v[144:145], off
	s_waitcnt vmcnt(6)
	s_setprio 1
	s_barrier
	v_mfma_f32_16x16x32_bf16 v[40:43], v[228:231], v[172:175], v[40:43]
	v_mfma_f32_16x16x32_bf16 v[28:31], v[236:239], v[172:175], v[28:31]
	v_mfma_f32_16x16x32_bf16 v[16:19], v[228:231], v[180:183], v[16:19]
	v_mfma_f32_16x16x32_bf16 v[8:11], v[236:239], v[180:183], v[8:11]
	v_mfma_f32_16x16x32_bf16 v[52:55], v[228:231], v[212:215], v[52:55]
	v_mfma_f32_16x16x32_bf16 v[48:51], v[236:239], v[212:215], v[48:51]
	v_mfma_f32_16x16x32_bf16 v[32:35], v[228:231], v[220:223], v[32:35]
	v_mfma_f32_16x16x32_bf16 v[24:27], v[236:239], v[220:223], v[24:27]
	v_mfma_f32_16x16x32_bf16 v[40:43], v[232:235], v[176:179], v[40:43]
	v_mfma_f32_16x16x32_bf16 v[28:31], v[240:243], v[176:179], v[28:31]
	v_mfma_f32_16x16x32_bf16 v[16:19], v[232:235], v[208:211], v[16:19]
	v_mfma_f32_16x16x32_bf16 v[8:11], v[240:243], v[208:211], v[8:11]
	v_mfma_f32_16x16x32_bf16 v[52:55], v[232:235], v[216:219], v[52:55]
	v_mfma_f32_16x16x32_bf16 v[48:51], v[240:243], v[216:219], v[48:51]
	v_mfma_f32_16x16x32_bf16 v[32:35], v[232:235], v[224:227], v[32:35]
	v_mfma_f32_16x16x32_bf16 v[24:27], v[240:243], v[224:227], v[24:27]
	s_barrier
	s_setprio 0
	s_add_i32 s40, s40, 2
	s_add_u32 s14, s14, 0x100
	s_addc_u32 s15, s15, 0
	s_add_u32 s38, s38, 0x100
	s_addc_u32 s39, s39, 0
	s_cmp_gt_u32 s40, 29
	s_cbranch_scc0 .LBB0_267
	s_and_b64 vcc, exec, s[6:7]
	s_cbranch_vccz .LBB0_270
	s_barrier

.LBB0_1002:
	s_add_u32 s22, s4, 0x80
	s_addc_u32 s23, s5, 0
	s_add_i32 s49, 0, 0x10000
	v_add_u32_e32 v84, s49, v181
	ds_read_b128 v[68:71], v84
	ds_read_b128 v[76:79], v84 offset:1024
	ds_read_b128 v[80:83], v84 offset:2048
	ds_read_b128 v[84:87], v84 offset:3072
	s_cmp_eq_u32 s48, 28
	s_cselect_b32 s25, s19, s23
	s_cselect_b32 s24, s18, s22
	s_cselect_b32 s23, s21, s47
	s_cselect_b32 s22, s20, s46
	v_lshl_add_u64 v[166:167], s[4:5], 0, v[164:165]
	s_add_i32 m0, s34, 0xc000
	ds_read_b128 v[144:147], v183
	ds_read_b128 v[148:151], v183 offset:1024
	ds_read_b128 v[172:175], v183 offset:2048
	ds_read_b128 v[176:179], v183 offset:3072
	ds_read_b128 v[208:211], v183 offset:4096
	ds_read_b128 v[212:215], v183 offset:5120
	ds_read_b128 v[216:219], v183 offset:6144
	ds_read_b128 v[220:223], v183 offset:7168
	global_load_lds_dwordx4 v[166:167], off
	v_lshl_add_u64 v[166:167], s[4:5], 0, v[162:163]
	s_add_i32 m0, s34, 0xe000
	s_nop 0
	global_load_lds_dwordx4 v[166:167], off
	s_waitcnt lgkmcnt(8)
	s_setprio 1
	s_barrier
	s_waitcnt lgkmcnt(0)
	v_mfma_f32_16x16x32_bf16 v[140:143], v[68:71], v[144:147], v[140:143]
	v_mfma_f32_16x16x32_bf16 v[136:139], v[80:83], v[144:147], v[136:139]
	v_mfma_f32_16x16x32_bf16 v[124:127], v[68:71], v[172:175], v[124:127]
	v_mfma_f32_16x16x32_bf16 v[120:123], v[80:83], v[172:175], v[120:123]
	v_mfma_f32_16x16x32_bf16 v[108:111], v[68:71], v[208:211], v[108:111]
	v_mfma_f32_16x16x32_bf16 v[104:107], v[80:83], v[208:211], v[104:107]
	v_mfma_f32_16x16x32_bf16 v[92:95], v[68:71], v[216:219], v[92:95]
	v_mfma_f32_16x16x32_bf16 v[88:91], v[80:83], v[216:219], v[88:91]
	v_mfma_f32_16x16x32_bf16 v[140:143], v[76:79], v[148:151], v[140:143]
	v_mfma_f32_16x16x32_bf16 v[136:139], v[84:87], v[148:151], v[136:139]
	v_mfma_f32_16x16x32_bf16 v[124:127], v[76:79], v[176:179], v[124:127]
	v_mfma_f32_16x16x32_bf16 v[120:123], v[84:87], v[176:179], v[120:123]
	v_mfma_f32_16x16x32_bf16 v[108:111], v[76:79], v[212:215], v[108:111]
	v_mfma_f32_16x16x32_bf16 v[104:107], v[84:87], v[212:215], v[104:107]
	v_mfma_f32_16x16x32_bf16 v[92:95], v[76:79], v[220:223], v[92:95]
	v_mfma_f32_16x16x32_bf16 v[88:91], v[84:87], v[220:223], v[88:91]
	s_barrier
	s_setprio 0
	s_add_i32 s52, 0, 0x14000
	v_add_u32_e32 v166, s52, v181
	s_add_i32 s49, s49, s31
	ds_read_b128 v[224:227], v166
	ds_read_b128 v[228:231], v166 offset:1024
	ds_read_b128 v[232:235], v166 offset:2048
	ds_read_b128 v[236:239], v166 offset:3072
	v_lshl_add_u64 v[166:167], s[22:23], 0, v[168:169]
	s_mov_b32 m0, s49
	v_lshl_add_u64 v[184:185], s[22:23], 0, v[156:157]
	global_load_lds_dwordx4 v[166:167], off
	s_add_i32 m0, s49, 0x2000
	s_nop 0
	global_load_lds_dwordx4 v[184:185], off
	s_setprio 1
	s_barrier
	s_waitcnt lgkmcnt(0)
	v_mfma_f32_16x16x32_bf16 v[132:135], v[224:227], v[144:147], v[132:135]
	v_mfma_f32_16x16x32_bf16 v[128:131], v[232:235], v[144:147], v[128:131]
	v_mfma_f32_16x16x32_bf16 v[116:119], v[224:227], v[172:175], v[116:119]
	v_mfma_f32_16x16x32_bf16 v[112:115], v[232:235], v[172:175], v[112:115]
	v_mfma_f32_16x16x32_bf16 v[100:103], v[224:227], v[208:211], v[100:103]
	v_mfma_f32_16x16x32_bf16 v[96:99], v[232:235], v[208:211], v[96:99]
	v_mfma_f32_16x16x32_bf16 v[72:75], v[224:227], v[216:219], v[72:75]
	v_mfma_f32_16x16x32_bf16 v[64:67], v[232:235], v[216:219], v[64:67]
	v_mfma_f32_16x16x32_bf16 v[132:135], v[228:231], v[148:151], v[132:135]
	v_mfma_f32_16x16x32_bf16 v[128:131], v[236:239], v[148:151], v[128:131]
	v_mfma_f32_16x16x32_bf16 v[116:119], v[228:231], v[176:179], v[116:119]
	v_mfma_f32_16x16x32_bf16 v[112:115], v[236:239], v[176:179], v[112:115]
	v_mfma_f32_16x16x32_bf16 v[100:103], v[228:231], v[212:215], v[100:103]
	v_mfma_f32_16x16x32_bf16 v[96:99], v[236:239], v[212:215], v[96:99]
	v_mfma_f32_16x16x32_bf16 v[72:75], v[228:231], v[220:223], v[72:75]
	v_mfma_f32_16x16x32_bf16 v[64:67], v[236:239], v[220:223], v[64:67]
	s_barrier
	s_setprio 0
	s_mov_b32 m0, s34
	v_lshl_add_u64 v[240:241], s[24:25], 0, v[152:153]
	ds_read_b128 v[144:147], v183 offset:16384
	ds_read_b128 v[148:151], v183 offset:17408
	ds_read_b128 v[172:175], v183 offset:18432
	ds_read_b128 v[176:179], v183 offset:19456
	ds_read_b128 v[208:211], v183 offset:20480
	ds_read_b128 v[212:215], v183 offset:21504
	ds_read_b128 v[216:219], v183 offset:22528
	ds_read_b128 v[220:223], v183 offset:23552
	global_load_lds_dwordx4 v[240:241], off
	v_lshl_add_u64 v[242:243], s[24:25], 0, v[158:159]
	s_mov_b32 m0, s35
	s_nop 0
	global_load_lds_dwordx4 v[242:243], off
	s_setprio 1
	s_barrier
	s_waitcnt lgkmcnt(0)
	v_mfma_f32_16x16x32_bf16 v[60:63], v[68:71], v[144:147], v[60:63]
	v_mfma_f32_16x16x32_bf16 v[56:59], v[80:83], v[144:147], v[56:59]
	v_mfma_f32_16x16x32_bf16 v[44:47], v[68:71], v[172:175], v[44:47]
	v_mfma_f32_16x16x32_bf16 v[40:43], v[80:83], v[172:175], v[40:43]
	v_mfma_f32_16x16x32_bf16 v[28:31], v[68:71], v[208:211], v[28:31]
	v_mfma_f32_16x16x32_bf16 v[20:23], v[80:83], v[208:211], v[20:23]
	v_mfma_f32_16x16x32_bf16 v[8:11], v[68:71], v[216:219], v[8:11]
	v_mfma_f32_16x16x32_bf16 v[0:3], v[80:83], v[216:219], v[0:3]
	v_mfma_f32_16x16x32_bf16 v[60:63], v[76:79], v[148:151], v[60:63]
	v_mfma_f32_16x16x32_bf16 v[56:59], v[84:87], v[148:151], v[56:59]
	v_mfma_f32_16x16x32_bf16 v[44:47], v[76:79], v[176:179], v[44:47]
	v_mfma_f32_16x16x32_bf16 v[40:43], v[84:87], v[176:179], v[40:43]
	v_mfma_f32_16x16x32_bf16 v[28:31], v[76:79], v[212:215], v[28:31]
	v_mfma_f32_16x16x32_bf16 v[20:23], v[84:87], v[212:215], v[20:23]
	v_mfma_f32_16x16x32_bf16 v[8:11], v[76:79], v[220:223], v[8:11]
	v_mfma_f32_16x16x32_bf16 v[0:3], v[84:87], v[220:223], v[0:3]
	s_barrier
	s_setprio 0
	s_add_u32 s50, s22, 0x80000
	s_addc_u32 s51, s23, 0
	s_add_i32 s49, s52, s31
	v_lshl_add_u64 v[68:69], s[50:51], 0, v[168:169]
	s_mov_b32 m0, s49
	s_nop 0
	global_load_lds_dwordx4 v[68:69], off
	v_lshl_add_u64 v[68:69], s[50:51], 0, v[156:157]
	s_add_i32 m0, s49, 0x2000
	s_nop 0
	global_load_lds_dwordx4 v[68:69], off
	s_waitcnt vmcnt(6)
	s_setprio 1
	s_barrier
	v_mfma_f32_16x16x32_bf16 v[52:55], v[224:227], v[144:147], v[52:55]
	v_mfma_f32_16x16x32_bf16 v[48:51], v[232:235], v[144:147], v[48:51]
	v_mfma_f32_16x16x32_bf16 v[36:39], v[224:227], v[172:175], v[36:39]
	v_mfma_f32_16x16x32_bf16 v[32:35], v[232:235], v[172:175], v[32:35]
	v_mfma_f32_16x16x32_bf16 v[24:27], v[224:227], v[208:211], v[24:27]
	v_mfma_f32_16x16x32_bf16 v[16:19], v[232:235], v[208:211], v[16:19]
	v_mfma_f32_16x16x32_bf16 v[12:15], v[224:227], v[216:219], v[12:15]
	v_mfma_f32_16x16x32_bf16 v[4:7], v[232:235], v[216:219], v[4:7]
	v_mfma_f32_16x16x32_bf16 v[52:55], v[228:231], v[148:151], v[52:55]
	v_mfma_f32_16x16x32_bf16 v[48:51], v[236:239], v[148:151], v[48:51]
	v_mfma_f32_16x16x32_bf16 v[36:39], v[228:231], v[176:179], v[36:39]
	v_mfma_f32_16x16x32_bf16 v[32:35], v[236:239], v[176:179], v[32:35]
	v_mfma_f32_16x16x32_bf16 v[24:27], v[228:231], v[212:215], v[24:27]
	v_mfma_f32_16x16x32_bf16 v[16:19], v[236:239], v[212:215], v[16:19]
	v_mfma_f32_16x16x32_bf16 v[12:15], v[228:231], v[220:223], v[12:15]
	v_mfma_f32_16x16x32_bf16 v[4:7], v[236:239], v[220:223], v[4:7]
	s_barrier
	s_setprio 0
	s_add_i32 s49, 0, 0x18000
	v_add_u32_e32 v84, s49, v181
	ds_read_b128 v[68:71], v84
	ds_read_b128 v[76:79], v84 offset:1024
	ds_read_b128 v[80:83], v84 offset:2048
	ds_read_b128 v[84:87], v84 offset:3072
	s_mov_b32 m0, s36
	v_lshl_add_u64 v[224:225], s[24:25], 0, v[154:155]
	ds_read_b128 v[144:147], v183 offset:32768
	ds_read_b128 v[148:151], v183 offset:33792
	ds_read_b128 v[172:175], v183 offset:34816
	ds_read_b128 v[176:179], v183 offset:35840
	ds_read_b128 v[208:211], v183 offset:36864
	ds_read_b128 v[212:215], v183 offset:37888
	ds_read_b128 v[216:219], v183 offset:38912
	ds_read_b128 v[220:223], v183 offset:39936
	global_load_lds_dwordx4 v[224:225], off
	v_lshl_add_u64 v[224:225], s[24:25], 0, v[160:161]
	s_mov_b32 m0, s37
	s_nop 0
	global_load_lds_dwordx4 v[224:225], off
	s_waitcnt lgkmcnt(8)
	s_setprio 1
	s_barrier
	s_waitcnt lgkmcnt(0)
	v_mfma_f32_16x16x32_bf16 v[140:143], v[68:71], v[144:147], v[140:143]
	v_mfma_f32_16x16x32_bf16 v[136:139], v[80:83], v[144:147], v[136:139]
	v_mfma_f32_16x16x32_bf16 v[124:127], v[68:71], v[172:175], v[124:127]
	v_mfma_f32_16x16x32_bf16 v[120:123], v[80:83], v[172:175], v[120:123]
	v_mfma_f32_16x16x32_bf16 v[108:111], v[68:71], v[208:211], v[108:111]
	v_mfma_f32_16x16x32_bf16 v[104:107], v[80:83], v[208:211], v[104:107]
	v_mfma_f32_16x16x32_bf16 v[92:95], v[68:71], v[216:219], v[92:95]
	v_mfma_f32_16x16x32_bf16 v[88:91], v[80:83], v[216:219], v[88:91]
	v_mfma_f32_16x16x32_bf16 v[140:143], v[76:79], v[148:151], v[140:143]
	v_mfma_f32_16x16x32_bf16 v[136:139], v[84:87], v[148:151], v[136:139]
	v_mfma_f32_16x16x32_bf16 v[124:127], v[76:79], v[176:179], v[124:127]
	v_mfma_f32_16x16x32_bf16 v[120:123], v[84:87], v[176:179], v[120:123]
	v_mfma_f32_16x16x32_bf16 v[108:111], v[76:79], v[212:215], v[108:111]
	v_mfma_f32_16x16x32_bf16 v[104:107], v[84:87], v[212:215], v[104:107]
	v_mfma_f32_16x16x32_bf16 v[92:95], v[76:79], v[220:223], v[92:95]
	v_mfma_f32_16x16x32_bf16 v[88:91], v[84:87], v[220:223], v[88:91]
	s_barrier
	s_setprio 0
	s_add_i32 s24, 0, 0x1c000
	s_add_i32 s25, s49, s31
	v_add_u32_e32 v170, s24, v181
	v_lshl_add_u64 v[166:167], v[166:167], 0, s[94:95]
	s_mov_b32 m0, s25
	ds_read_b128 v[224:227], v170
	ds_read_b128 v[228:231], v170 offset:1024
	ds_read_b128 v[232:235], v170 offset:2048
	ds_read_b128 v[236:239], v170 offset:3072
	global_load_lds_dwordx4 v[166:167], off
	v_lshl_add_u64 v[166:167], v[184:185], 0, s[94:95]
	s_add_i32 m0, s25, 0x2000
	s_nop 0
	global_load_lds_dwordx4 v[166:167], off
	s_setprio 1
	s_barrier
	s_waitcnt lgkmcnt(0)
	v_mfma_f32_16x16x32_bf16 v[132:135], v[224:227], v[144:147], v[132:135]
	v_mfma_f32_16x16x32_bf16 v[128:131], v[232:235], v[144:147], v[128:131]
	v_mfma_f32_16x16x32_bf16 v[116:119], v[224:227], v[172:175], v[116:119]
	v_mfma_f32_16x16x32_bf16 v[112:115], v[232:235], v[172:175], v[112:115]
	v_mfma_f32_16x16x32_bf16 v[100:103], v[224:227], v[208:211], v[100:103]
	v_mfma_f32_16x16x32_bf16 v[96:99], v[232:235], v[208:211], v[96:99]
	v_mfma_f32_16x16x32_bf16 v[72:75], v[224:227], v[216:219], v[72:75]
	v_mfma_f32_16x16x32_bf16 v[64:67], v[232:235], v[216:219], v[64:67]
	v_mfma_f32_16x16x32_bf16 v[132:135], v[228:231], v[148:151], v[132:135]
	v_mfma_f32_16x16x32_bf16 v[128:131], v[236:239], v[148:151], v[128:131]
	v_mfma_f32_16x16x32_bf16 v[116:119], v[228:231], v[176:179], v[116:119]
	v_mfma_f32_16x16x32_bf16 v[112:115], v[236:239], v[176:179], v[112:115]
	v_mfma_f32_16x16x32_bf16 v[100:103], v[228:231], v[212:215], v[100:103]
	v_mfma_f32_16x16x32_bf16 v[96:99], v[236:239], v[212:215], v[96:99]
	v_mfma_f32_16x16x32_bf16 v[72:75], v[228:231], v[220:223], v[72:75]
	v_mfma_f32_16x16x32_bf16 v[64:67], v[236:239], v[220:223], v[64:67]
	s_barrier
	s_setprio 0
	s_mov_b32 m0, s40
	v_lshl_add_u64 v[166:167], v[240:241], 0, s[94:95]
	ds_read_b128 v[144:147], v183 offset:49152
	ds_read_b128 v[148:151], v183 offset:50176
	ds_read_b128 v[172:175], v183 offset:51200
	ds_read_b128 v[176:179], v183 offset:52224
	ds_read_b128 v[208:211], v183 offset:53248
	ds_read_b128 v[212:215], v183 offset:54272
	ds_read_b128 v[216:219], v183 offset:55296
	ds_read_b128 v[220:223], v183 offset:56320
	global_load_lds_dwordx4 v[166:167], off
	v_lshl_add_u64 v[166:167], v[242:243], 0, s[94:95]
	s_mov_b32 m0, s41
	s_nop 0
	global_load_lds_dwordx4 v[166:167], off
	s_setprio 1
	s_barrier
	s_waitcnt lgkmcnt(0)
	v_mfma_f32_16x16x32_bf16 v[60:63], v[68:71], v[144:147], v[60:63]
	v_mfma_f32_16x16x32_bf16 v[56:59], v[80:83], v[144:147], v[56:59]
	v_mfma_f32_16x16x32_bf16 v[44:47], v[68:71], v[172:175], v[44:47]
	v_mfma_f32_16x16x32_bf16 v[40:43], v[80:83], v[172:175], v[40:43]
	v_mfma_f32_16x16x32_bf16 v[28:31], v[68:71], v[208:211], v[28:31]
	v_mfma_f32_16x16x32_bf16 v[20:23], v[80:83], v[208:211], v[20:23]
	v_mfma_f32_16x16x32_bf16 v[8:11], v[68:71], v[216:219], v[8:11]
	v_mfma_f32_16x16x32_bf16 v[0:3], v[80:83], v[216:219], v[0:3]
	v_mfma_f32_16x16x32_bf16 v[60:63], v[76:79], v[148:151], v[60:63]
	v_mfma_f32_16x16x32_bf16 v[56:59], v[84:87], v[148:151], v[56:59]
	v_mfma_f32_16x16x32_bf16 v[44:47], v[76:79], v[176:179], v[44:47]
	v_mfma_f32_16x16x32_bf16 v[40:43], v[84:87], v[176:179], v[40:43]
	v_mfma_f32_16x16x32_bf16 v[28:31], v[76:79], v[212:215], v[28:31]
	v_mfma_f32_16x16x32_bf16 v[20:23], v[84:87], v[212:215], v[20:23]
	v_mfma_f32_16x16x32_bf16 v[8:11], v[76:79], v[220:223], v[8:11]
	v_mfma_f32_16x16x32_bf16 v[0:3], v[84:87], v[220:223], v[0:3]
	s_barrier
	s_setprio 0
	s_add_u32 s22, s22, 0x80080
	s_addc_u32 s23, s23, 0
	s_add_i32 s24, s24, s31
	v_lshl_add_u64 v[68:69], s[22:23], 0, v[168:169]
	s_mov_b32 m0, s24
	s_nop 0
	global_load_lds_dwordx4 v[68:69], off
	v_lshl_add_u64 v[68:69], s[22:23], 0, v[156:157]
	s_add_i32 m0, s24, 0x2000
	s_nop 0
	global_load_lds_dwordx4 v[68:69], off
	s_waitcnt vmcnt(6)
	s_setprio 1
	s_barrier
	v_mfma_f32_16x16x32_bf16 v[52:55], v[224:227], v[144:147], v[52:55]
	v_mfma_f32_16x16x32_bf16 v[48:51], v[232:235], v[144:147], v[48:51]
	v_mfma_f32_16x16x32_bf16 v[36:39], v[224:227], v[172:175], v[36:39]
	v_mfma_f32_16x16x32_bf16 v[32:35], v[232:235], v[172:175], v[32:35]
	v_mfma_f32_16x16x32_bf16 v[24:27], v[224:227], v[208:211], v[24:27]
	v_mfma_f32_16x16x32_bf16 v[16:19], v[232:235], v[208:211], v[16:19]
	v_mfma_f32_16x16x32_bf16 v[12:15], v[224:227], v[216:219], v[12:15]
	v_mfma_f32_16x16x32_bf16 v[4:7], v[232:235], v[216:219], v[4:7]
	v_mfma_f32_16x16x32_bf16 v[52:55], v[228:231], v[148:151], v[52:55]
	v_mfma_f32_16x16x32_bf16 v[48:51], v[236:239], v[148:151], v[48:51]
	v_mfma_f32_16x16x32_bf16 v[36:39], v[228:231], v[176:179], v[36:39]
	v_mfma_f32_16x16x32_bf16 v[32:35], v[236:239], v[176:179], v[32:35]
	v_mfma_f32_16x16x32_bf16 v[24:27], v[228:231], v[212:215], v[24:27]
	v_mfma_f32_16x16x32_bf16 v[16:19], v[236:239], v[212:215], v[16:19]
	v_mfma_f32_16x16x32_bf16 v[12:15], v[228:231], v[220:223], v[12:15]
	v_mfma_f32_16x16x32_bf16 v[4:7], v[236:239], v[220:223], v[4:7]
	s_barrier
	s_setprio 0
	s_add_i32 s48, s48, 2
	s_add_u32 s4, s4, 0x100
	s_addc_u32 s5, s5, 0
	s_add_u32 s46, s46, 0x100
	s_addc_u32 s47, s47, 0
	s_cmp_gt_u32 s48, 29
	s_cbranch_scc0 .LBB0_1002
	s_and_b64 vcc, exec, s[14:15]
	s_cbranch_vccz .LBB0_1005
	s_barrier

.LBB0_1423:
	s_add_u32 s36, s26, s34
	s_addc_u32 s37, s27, s35
	s_add_u32 s38, s36, 0x100
	s_addc_u32 s39, s37, 0
	s_add_u32 s58, s23, s34
	s_addc_u32 s59, s56, s35
	s_add_i32 s60, 0, 0x10000
	v_add_u32_e32 v141, s60, v135
	ds_read_b128 v[158:161], v141
	ds_read_b128 v[162:165], v141 offset:1024
	ds_read_b128 v[172:175], v141 offset:2048
	ds_read_b128 v[176:179], v141 offset:3072
	s_cmpk_eq_i32 s34, 0xf00
	s_cselect_b64 vcc, -1, 0
	s_and_b64 s[36:37], vcc, exec
	v_cndmask_b32_e32 v168, v134, v154, vcc
	v_cndmask_b32_e32 v166, v132, v155, vcc
	v_cndmask_b32_e32 v129, v128, v153, vcc
	v_cndmask_b32_e32 v139, v138, v156, vcc
	s_cselect_b32 s39, s31, s39
	s_cselect_b32 s38, s30, s38
	s_cselect_b32 s37, s5, s59
	s_cselect_b32 s36, s4, s58
	v_lshl_add_u64 v[184:185], v[144:145], 0, s[34:35]
	s_add_i32 m0, s43, 0xc000
	ds_read_b128 v[180:183], v152
	ds_read_b128 v[208:211], v152 offset:1024
	ds_read_b128 v[212:215], v152 offset:2048
	ds_read_b128 v[216:219], v152 offset:3072
	ds_read_b128 v[220:223], v152 offset:4096
	ds_read_b128 v[224:227], v152 offset:5120
	ds_read_b128 v[228:231], v152 offset:6144
	ds_read_b128 v[232:235], v152 offset:7168
	global_load_lds_dwordx4 v[184:185], off
	v_lshl_add_u64 v[184:185], v[142:143], 0, s[34:35]
	s_add_i32 m0, s43, 0xe000
	s_nop 0
	global_load_lds_dwordx4 v[184:185], off
	s_waitcnt lgkmcnt(8)
	s_setprio 1
	s_barrier
	s_waitcnt lgkmcnt(0)
	v_mfma_f32_16x16x32_bf16 v[124:127], v[158:161], v[180:183], v[124:127]
	v_mfma_f32_16x16x32_bf16 v[120:123], v[172:175], v[180:183], v[120:123]
	v_mfma_f32_16x16x32_bf16 v[116:119], v[158:161], v[212:215], v[116:119]
	v_mfma_f32_16x16x32_bf16 v[112:115], v[172:175], v[212:215], v[112:115]
	v_mfma_f32_16x16x32_bf16 v[108:111], v[158:161], v[220:223], v[108:111]
	v_mfma_f32_16x16x32_bf16 v[104:107], v[172:175], v[220:223], v[104:107]
	v_mfma_f32_16x16x32_bf16 v[100:103], v[158:161], v[228:231], v[100:103]
	v_mfma_f32_16x16x32_bf16 v[96:99], v[172:175], v[228:231], v[96:99]
	v_mfma_f32_16x16x32_bf16 v[124:127], v[162:165], v[208:211], v[124:127]
	v_mfma_f32_16x16x32_bf16 v[120:123], v[176:179], v[208:211], v[120:123]
	v_mfma_f32_16x16x32_bf16 v[116:119], v[162:165], v[216:219], v[116:119]
	v_mfma_f32_16x16x32_bf16 v[112:115], v[176:179], v[216:219], v[112:115]
	v_mfma_f32_16x16x32_bf16 v[108:111], v[162:165], v[224:227], v[108:111]
	v_mfma_f32_16x16x32_bf16 v[104:107], v[176:179], v[224:227], v[104:107]
	v_mfma_f32_16x16x32_bf16 v[100:103], v[162:165], v[232:235], v[100:103]
	v_mfma_f32_16x16x32_bf16 v[96:99], v[176:179], v[232:235], v[96:99]
	s_barrier
	s_setprio 0
	s_add_i32 s61, 0, 0x14000
	s_add_i32 s58, s60, s9
	v_add_u32_e32 v141, s61, v135
	v_lshl_add_u64 v[184:185], s[36:37], 0, v[130:131]
	s_mov_b32 m0, s58
	ds_read_b128 v[236:239], v141
	ds_read_b128 v[240:243], v141 offset:1024
	ds_read_b128 v[244:247], v141 offset:2048
	ds_read_b128 v[248:251], v141 offset:3072
	global_load_lds_dwordx4 v[184:185], off
	v_lshl_add_u64 v[188:189], s[36:37], 0, v[136:137]
	s_add_i32 m0, s58, 0x2000
	s_nop 0
	global_load_lds_dwordx4 v[188:189], off
	s_setprio 1
	s_barrier
	s_waitcnt lgkmcnt(0)
	v_mfma_f32_16x16x32_bf16 v[92:95], v[236:239], v[180:183], v[92:95]
	v_mfma_f32_16x16x32_bf16 v[88:91], v[244:247], v[180:183], v[88:91]
	v_mfma_f32_16x16x32_bf16 v[84:87], v[236:239], v[212:215], v[84:87]
	v_mfma_f32_16x16x32_bf16 v[80:83], v[244:247], v[212:215], v[80:83]
	v_mfma_f32_16x16x32_bf16 v[76:79], v[236:239], v[220:223], v[76:79]
	v_mfma_f32_16x16x32_bf16 v[72:75], v[244:247], v[220:223], v[72:75]
	v_mfma_f32_16x16x32_bf16 v[68:71], v[236:239], v[228:231], v[68:71]
	v_mfma_f32_16x16x32_bf16 v[64:67], v[244:247], v[228:231], v[64:67]
	v_mfma_f32_16x16x32_bf16 v[92:95], v[240:243], v[208:211], v[92:95]
	v_mfma_f32_16x16x32_bf16 v[88:91], v[248:251], v[208:211], v[88:91]
	v_mfma_f32_16x16x32_bf16 v[84:87], v[240:243], v[216:219], v[84:87]
	v_mfma_f32_16x16x32_bf16 v[80:83], v[248:251], v[216:219], v[80:83]
	v_mfma_f32_16x16x32_bf16 v[76:79], v[240:243], v[224:227], v[76:79]
	v_mfma_f32_16x16x32_bf16 v[72:75], v[248:251], v[224:227], v[72:75]
	v_mfma_f32_16x16x32_bf16 v[68:71], v[240:243], v[232:235], v[68:71]
	v_mfma_f32_16x16x32_bf16 v[64:67], v[248:251], v[232:235], v[64:67]
	s_barrier
	s_setprio 0
	s_mov_b32 m0, s43
	ds_read_b128 v[180:183], v152 offset:16384
	ds_read_b128 v[208:211], v152 offset:17408
	ds_read_b128 v[212:215], v152 offset:18432
	ds_read_b128 v[216:219], v152 offset:19456
	ds_read_b128 v[220:223], v152 offset:20480
	ds_read_b128 v[224:227], v152 offset:21504
	ds_read_b128 v[228:231], v152 offset:22528
	ds_read_b128 v[232:235], v152 offset:23552
	global_load_lds_dwordx4 v168, s[38:39]
	s_mov_b32 m0, s44
	v_mov_b32_e32 v167, v169
	global_load_lds_dwordx4 v166, s[38:39]
	v_lshl_add_u64 v[170:171], s[38:39], 0, v[168:169]
	v_lshl_add_u64 v[166:167], s[38:39], 0, v[166:167]
	s_setprio 1
	s_barrier
	s_waitcnt lgkmcnt(0)
	v_mfma_f32_16x16x32_bf16 v[60:63], v[158:161], v[180:183], v[60:63]
	v_mfma_f32_16x16x32_bf16 v[56:59], v[172:175], v[180:183], v[56:59]
	v_mfma_f32_16x16x32_bf16 v[52:55], v[158:161], v[212:215], v[52:55]
	v_mfma_f32_16x16x32_bf16 v[48:51], v[172:175], v[212:215], v[48:51]
	v_mfma_f32_16x16x32_bf16 v[44:47], v[158:161], v[220:223], v[44:47]
	v_mfma_f32_16x16x32_bf16 v[40:43], v[172:175], v[220:223], v[40:43]
	v_mfma_f32_16x16x32_bf16 v[36:39], v[158:161], v[228:231], v[36:39]
	v_mfma_f32_16x16x32_bf16 v[32:35], v[172:175], v[228:231], v[32:35]
	v_mfma_f32_16x16x32_bf16 v[60:63], v[162:165], v[208:211], v[60:63]
	v_mfma_f32_16x16x32_bf16 v[56:59], v[176:179], v[208:211], v[56:59]
	v_mfma_f32_16x16x32_bf16 v[52:55], v[162:165], v[216:219], v[52:55]
	v_mfma_f32_16x16x32_bf16 v[48:51], v[176:179], v[216:219], v[48:51]
	v_mfma_f32_16x16x32_bf16 v[44:47], v[162:165], v[224:227], v[44:47]
	v_mfma_f32_16x16x32_bf16 v[40:43], v[176:179], v[224:227], v[40:43]
	v_mfma_f32_16x16x32_bf16 v[36:39], v[162:165], v[232:235], v[36:39]
	v_mfma_f32_16x16x32_bf16 v[32:35], v[176:179], v[232:235], v[32:35]
	s_barrier
	s_setprio 0
	s_add_u32 s58, s36, 0x80000
	s_addc_u32 s59, s37, 0
	s_add_i32 s60, s61, s9
	v_lshl_add_u64 v[158:159], s[58:59], 0, v[130:131]
	s_mov_b32 m0, s60
	s_nop 0
	global_load_lds_dwordx4 v[158:159], off
	v_lshl_add_u64 v[158:159], s[58:59], 0, v[136:137]
	s_add_i32 m0, s60, 0x2000
	s_nop 0
	global_load_lds_dwordx4 v[158:159], off
	s_waitcnt vmcnt(6)
	s_setprio 1
	s_barrier
	v_mfma_f32_16x16x32_bf16 v[28:31], v[236:239], v[180:183], v[28:31]
	v_mfma_f32_16x16x32_bf16 v[24:27], v[244:247], v[180:183], v[24:27]
	v_mfma_f32_16x16x32_bf16 v[20:23], v[236:239], v[212:215], v[20:23]
	v_mfma_f32_16x16x32_bf16 v[16:19], v[244:247], v[212:215], v[16:19]
	v_mfma_f32_16x16x32_bf16 v[12:15], v[236:239], v[220:223], v[12:15]
	v_mfma_f32_16x16x32_bf16 v[8:11], v[244:247], v[220:223], v[8:11]
	v_mfma_f32_16x16x32_bf16 v[4:7], v[236:239], v[228:231], v[4:7]
	v_mfma_f32_16x16x32_bf16 v[0:3], v[244:247], v[228:231], v[0:3]
	v_mfma_f32_16x16x32_bf16 v[28:31], v[240:243], v[208:211], v[28:31]
	v_mfma_f32_16x16x32_bf16 v[24:27], v[248:251], v[208:211], v[24:27]
	v_mfma_f32_16x16x32_bf16 v[20:23], v[240:243], v[216:219], v[20:23]
	v_mfma_f32_16x16x32_bf16 v[16:19], v[248:251], v[216:219], v[16:19]
	v_mfma_f32_16x16x32_bf16 v[12:15], v[240:243], v[224:227], v[12:15]
	v_mfma_f32_16x16x32_bf16 v[8:11], v[248:251], v[224:227], v[8:11]
	v_mfma_f32_16x16x32_bf16 v[4:7], v[240:243], v[232:235], v[4:7]
	v_mfma_f32_16x16x32_bf16 v[0:3], v[248:251], v[232:235], v[0:3]
	s_barrier
	s_setprio 0
	s_add_i32 s58, 0, 0x18000
	v_add_u32_e32 v141, s58, v135
	ds_read_b128 v[158:161], v141
	ds_read_b128 v[162:165], v141 offset:1024
	ds_read_b128 v[172:175], v141 offset:2048
	ds_read_b128 v[176:179], v141 offset:3072
	s_mov_b32 m0, s45
	ds_read_b128 v[180:183], v152 offset:32768
	ds_read_b128 v[208:211], v152 offset:33792
	ds_read_b128 v[212:215], v152 offset:34816
	ds_read_b128 v[216:219], v152 offset:35840
	ds_read_b128 v[220:223], v152 offset:36864
	ds_read_b128 v[224:227], v152 offset:37888
	ds_read_b128 v[228:231], v152 offset:38912
	ds_read_b128 v[232:235], v152 offset:39936
	global_load_lds_dwordx4 v129, s[38:39]
	s_mov_b32 m0, s46
	s_nop 0
	global_load_lds_dwordx4 v139, s[38:39]
	s_waitcnt lgkmcnt(8)
	s_setprio 1
	s_barrier
	s_waitcnt lgkmcnt(0)
	v_mfma_f32_16x16x32_bf16 v[124:127], v[158:161], v[180:183], v[124:127]
	v_mfma_f32_16x16x32_bf16 v[120:123], v[172:175], v[180:183], v[120:123]
	v_mfma_f32_16x16x32_bf16 v[116:119], v[158:161], v[212:215], v[116:119]
	v_mfma_f32_16x16x32_bf16 v[112:115], v[172:175], v[212:215], v[112:115]
	v_mfma_f32_16x16x32_bf16 v[108:111], v[158:161], v[220:223], v[108:111]
	v_mfma_f32_16x16x32_bf16 v[104:107], v[172:175], v[220:223], v[104:107]
	v_mfma_f32_16x16x32_bf16 v[100:103], v[158:161], v[228:231], v[100:103]
	v_mfma_f32_16x16x32_bf16 v[96:99], v[172:175], v[228:231], v[96:99]
	v_mfma_f32_16x16x32_bf16 v[124:127], v[162:165], v[208:211], v[124:127]
	v_mfma_f32_16x16x32_bf16 v[120:123], v[176:179], v[208:211], v[120:123]
	v_mfma_f32_16x16x32_bf16 v[116:119], v[162:165], v[216:219], v[116:119]
	v_mfma_f32_16x16x32_bf16 v[112:115], v[176:179], v[216:219], v[112:115]
	v_mfma_f32_16x16x32_bf16 v[108:111], v[162:165], v[224:227], v[108:111]
	v_mfma_f32_16x16x32_bf16 v[104:107], v[176:179], v[224:227], v[104:107]
	v_mfma_f32_16x16x32_bf16 v[100:103], v[162:165], v[232:235], v[100:103]
	v_mfma_f32_16x16x32_bf16 v[96:99], v[176:179], v[232:235], v[96:99]
	s_barrier
	s_setprio 0
	s_add_i32 s38, 0, 0x1c000
	s_add_i32 s39, s58, s9
	v_add_u32_e32 v129, s38, v135
	v_lshl_add_u64 v[184:185], v[184:185], 0, s[94:95]
	s_mov_b32 m0, s39
	ds_read_b128 v[236:239], v129
	ds_read_b128 v[240:243], v129 offset:1024
	ds_read_b128 v[244:247], v129 offset:2048
	ds_read_b128 v[248:251], v129 offset:3072
	global_load_lds_dwordx4 v[184:185], off
	v_lshl_add_u64 v[184:185], v[188:189], 0, s[94:95]
	s_add_i32 m0, s39, 0x2000
	s_nop 0
	global_load_lds_dwordx4 v[184:185], off
	s_setprio 1
	s_barrier
	s_waitcnt lgkmcnt(0)
	v_mfma_f32_16x16x32_bf16 v[92:95], v[236:239], v[180:183], v[92:95]
	v_mfma_f32_16x16x32_bf16 v[88:91], v[244:247], v[180:183], v[88:91]
	v_mfma_f32_16x16x32_bf16 v[84:87], v[236:239], v[212:215], v[84:87]
	v_mfma_f32_16x16x32_bf16 v[80:83], v[244:247], v[212:215], v[80:83]
	v_mfma_f32_16x16x32_bf16 v[76:79], v[236:239], v[220:223], v[76:79]
	v_mfma_f32_16x16x32_bf16 v[72:75], v[244:247], v[220:223], v[72:75]
	v_mfma_f32_16x16x32_bf16 v[68:71], v[236:239], v[228:231], v[68:71]
	v_mfma_f32_16x16x32_bf16 v[64:67], v[244:247], v[228:231], v[64:67]
	v_mfma_f32_16x16x32_bf16 v[92:95], v[240:243], v[208:211], v[92:95]
	v_mfma_f32_16x16x32_bf16 v[88:91], v[248:251], v[208:211], v[88:91]
	v_mfma_f32_16x16x32_bf16 v[84:87], v[240:243], v[216:219], v[84:87]
	v_mfma_f32_16x16x32_bf16 v[80:83], v[248:251], v[216:219], v[80:83]
	v_mfma_f32_16x16x32_bf16 v[76:79], v[240:243], v[224:227], v[76:79]
	v_mfma_f32_16x16x32_bf16 v[72:75], v[248:251], v[224:227], v[72:75]
	v_mfma_f32_16x16x32_bf16 v[68:71], v[240:243], v[232:235], v[68:71]
	v_mfma_f32_16x16x32_bf16 v[64:67], v[248:251], v[232:235], v[64:67]
	s_barrier
	s_setprio 0
	s_mov_b32 m0, s47
	v_lshl_add_u64 v[170:171], v[170:171], 0, s[94:95]
	ds_read_b128 v[180:183], v152 offset:49152
	ds_read_b128 v[208:211], v152 offset:50176
	ds_read_b128 v[212:215], v152 offset:51200
	ds_read_b128 v[216:219], v152 offset:52224
	ds_read_b128 v[220:223], v152 offset:53248
	ds_read_b128 v[224:227], v152 offset:54272
	ds_read_b128 v[228:231], v152 offset:55296
	ds_read_b128 v[232:235], v152 offset:56320
	global_load_lds_dwordx4 v[170:171], off
	v_lshl_add_u64 v[166:167], v[166:167], 0, s[94:95]
	s_mov_b32 m0, s48
	s_nop 0
	global_load_lds_dwordx4 v[166:167], off
	s_setprio 1
	s_barrier
	s_waitcnt lgkmcnt(0)
	v_mfma_f32_16x16x32_bf16 v[60:63], v[158:161], v[180:183], v[60:63]
	v_mfma_f32_16x16x32_bf16 v[56:59], v[172:175], v[180:183], v[56:59]
	v_mfma_f32_16x16x32_bf16 v[52:55], v[158:161], v[212:215], v[52:55]
	v_mfma_f32_16x16x32_bf16 v[48:51], v[172:175], v[212:215], v[48:51]
	v_mfma_f32_16x16x32_bf16 v[44:47], v[158:161], v[220:223], v[44:47]
	v_mfma_f32_16x16x32_bf16 v[40:43], v[172:175], v[220:223], v[40:43]
	v_mfma_f32_16x16x32_bf16 v[36:39], v[158:161], v[228:231], v[36:39]
	v_mfma_f32_16x16x32_bf16 v[32:35], v[172:175], v[228:231], v[32:35]
	v_mfma_f32_16x16x32_bf16 v[60:63], v[162:165], v[208:211], v[60:63]
	v_mfma_f32_16x16x32_bf16 v[56:59], v[176:179], v[208:211], v[56:59]
	v_mfma_f32_16x16x32_bf16 v[52:55], v[162:165], v[216:219], v[52:55]
	v_mfma_f32_16x16x32_bf16 v[48:51], v[176:179], v[216:219], v[48:51]
	v_mfma_f32_16x16x32_bf16 v[44:47], v[162:165], v[224:227], v[44:47]
	v_mfma_f32_16x16x32_bf16 v[40:43], v[176:179], v[224:227], v[40:43]
	v_mfma_f32_16x16x32_bf16 v[36:39], v[162:165], v[232:235], v[36:39]
	v_mfma_f32_16x16x32_bf16 v[32:35], v[176:179], v[232:235], v[32:35]
	s_barrier
	s_setprio 0
	s_add_u32 s36, s36, 0x80080
	s_addc_u32 s37, s37, 0
	s_add_i32 s38, s38, s9
	v_lshl_add_u64 v[158:159], s[36:37], 0, v[130:131]
	s_mov_b32 m0, s38
	s_nop 0
	global_load_lds_dwordx4 v[158:159], off
	v_lshl_add_u64 v[158:159], s[36:37], 0, v[136:137]
	s_add_i32 m0, s38, 0x2000
	s_nop 0
	global_load_lds_dwordx4 v[158:159], off
	s_waitcnt vmcnt(6)
	s_setprio 1
	s_barrier
	v_mfma_f32_16x16x32_bf16 v[28:31], v[236:239], v[180:183], v[28:31]
	v_mfma_f32_16x16x32_bf16 v[24:27], v[244:247], v[180:183], v[24:27]
	v_mfma_f32_16x16x32_bf16 v[20:23], v[236:239], v[212:215], v[20:23]
	v_mfma_f32_16x16x32_bf16 v[16:19], v[244:247], v[212:215], v[16:19]
	v_mfma_f32_16x16x32_bf16 v[12:15], v[236:239], v[220:223], v[12:15]
	v_mfma_f32_16x16x32_bf16 v[8:11], v[244:247], v[220:223], v[8:11]
	v_mfma_f32_16x16x32_bf16 v[4:7], v[236:239], v[228:231], v[4:7]
	v_mfma_f32_16x16x32_bf16 v[0:3], v[244:247], v[228:231], v[0:3]
	v_mfma_f32_16x16x32_bf16 v[28:31], v[240:243], v[208:211], v[28:31]
	v_mfma_f32_16x16x32_bf16 v[24:27], v[248:251], v[208:211], v[24:27]
	v_mfma_f32_16x16x32_bf16 v[20:23], v[240:243], v[216:219], v[20:23]
	v_mfma_f32_16x16x32_bf16 v[16:19], v[248:251], v[216:219], v[16:19]
	v_mfma_f32_16x16x32_bf16 v[12:15], v[240:243], v[224:227], v[12:15]
	v_mfma_f32_16x16x32_bf16 v[8:11], v[248:251], v[224:227], v[8:11]
	v_mfma_f32_16x16x32_bf16 v[4:7], v[240:243], v[232:235], v[4:7]
	v_mfma_f32_16x16x32_bf16 v[0:3], v[248:251], v[232:235], v[0:3]
	s_barrier
	s_setprio 0
	s_add_i32 s57, s57, 2
	s_add_u32 s34, s34, 0x100
	s_addc_u32 s35, s35, 0
	s_cmp_gt_u32 s57, 29
	s_cbranch_scc0 .LBB0_1423
	s_and_b64 vcc, exec, s[16:17]
	s_cbranch_vccz .LBB0_1426
	s_barrier

.LBB0_1521:
	s_add_u32 s26, s24, 0x80
	s_addc_u32 s27, s25, 0
	s_add_i32 s57, 0, 0x10000
	v_add_u32_e32 v147, s57, v145
	ds_read_b128 v[148:151], v147
	ds_read_b128 v[152:155], v147 offset:1024
	ds_read_b128 v[156:159], v147 offset:2048
	ds_read_b128 v[160:163], v147 offset:3072
	s_cmp_eq_u32 s56, 4
	s_cselect_b32 s29, s17, s27
	s_cselect_b32 s28, s21, s26
	s_cselect_b32 s27, s30, s35
	s_cselect_b32 s26, s31, s34
	v_lshl_add_u64 v[170:171], s[24:25], 0, v[142:143]
	s_add_i32 m0, s43, 0xc000
	ds_read_b128 v[164:167], v146
	ds_read_b128 v[172:175], v146 offset:1024
	ds_read_b128 v[176:179], v146 offset:2048
	ds_read_b128 v[180:183], v146 offset:3072
	ds_read_b128 v[208:211], v146 offset:4096
	ds_read_b128 v[212:215], v146 offset:5120
	ds_read_b128 v[216:219], v146 offset:6144
	ds_read_b128 v[220:223], v146 offset:7168
	global_load_lds_dwordx4 v[170:171], off
	v_lshl_add_u64 v[170:171], s[24:25], 0, v[140:141]
	s_add_i32 m0, s43, 0xe000
	s_nop 0
	global_load_lds_dwordx4 v[170:171], off
	s_waitcnt lgkmcnt(8)
	s_setprio 1
	s_barrier
	s_waitcnt lgkmcnt(0)
	v_mfma_f32_16x16x32_bf16 v[124:127], v[148:151], v[164:167], v[124:127]
	v_mfma_f32_16x16x32_bf16 v[120:123], v[156:159], v[164:167], v[120:123]
	v_mfma_f32_16x16x32_bf16 v[112:115], v[148:151], v[176:179], v[112:115]
	v_mfma_f32_16x16x32_bf16 v[104:107], v[156:159], v[176:179], v[104:107]
	v_mfma_f32_16x16x32_bf16 v[96:99], v[148:151], v[208:211], v[96:99]
	v_mfma_f32_16x16x32_bf16 v[88:91], v[156:159], v[208:211], v[88:91]
	v_mfma_f32_16x16x32_bf16 v[80:83], v[148:151], v[216:219], v[80:83]
	v_mfma_f32_16x16x32_bf16 v[72:75], v[156:159], v[216:219], v[72:75]
	v_mfma_f32_16x16x32_bf16 v[124:127], v[152:155], v[172:175], v[124:127]
	v_mfma_f32_16x16x32_bf16 v[120:123], v[160:163], v[172:175], v[120:123]
	v_mfma_f32_16x16x32_bf16 v[112:115], v[152:155], v[180:183], v[112:115]
	v_mfma_f32_16x16x32_bf16 v[104:107], v[160:163], v[180:183], v[104:107]
	v_mfma_f32_16x16x32_bf16 v[96:99], v[152:155], v[212:215], v[96:99]
	v_mfma_f32_16x16x32_bf16 v[88:91], v[160:163], v[212:215], v[88:91]
	v_mfma_f32_16x16x32_bf16 v[80:83], v[152:155], v[220:223], v[80:83]
	v_mfma_f32_16x16x32_bf16 v[72:75], v[160:163], v[220:223], v[72:75]
	s_barrier
	s_setprio 0
	s_add_i32 s60, 0, 0x14000
	s_add_i32 s57, s57, s42
	v_add_u32_e32 v147, s60, v145
	v_lshl_add_u64 v[170:171], s[26:27], 0, v[168:169]
	s_mov_b32 m0, s57
	ds_read_b128 v[224:227], v147
	ds_read_b128 v[228:231], v147 offset:1024
	ds_read_b128 v[232:235], v147 offset:2048
	ds_read_b128 v[236:239], v147 offset:3072
	global_load_lds_dwordx4 v[170:171], off
	v_lshl_add_u64 v[184:185], s[26:27], 0, v[132:133]
	s_add_i32 m0, s57, 0x2000
	s_nop 0
	global_load_lds_dwordx4 v[184:185], off
	s_setprio 1
	s_barrier
	s_waitcnt lgkmcnt(0)
	v_mfma_f32_16x16x32_bf16 v[116:119], v[224:227], v[164:167], v[116:119]
	v_mfma_f32_16x16x32_bf16 v[108:111], v[232:235], v[164:167], v[108:111]
	v_mfma_f32_16x16x32_bf16 v[100:103], v[224:227], v[176:179], v[100:103]
	v_mfma_f32_16x16x32_bf16 v[92:95], v[232:235], v[176:179], v[92:95]
	v_mfma_f32_16x16x32_bf16 v[84:87], v[224:227], v[208:211], v[84:87]
	v_mfma_f32_16x16x32_bf16 v[76:79], v[232:235], v[208:211], v[76:79]
	v_mfma_f32_16x16x32_bf16 v[68:71], v[224:227], v[216:219], v[68:71]
	v_mfma_f32_16x16x32_bf16 v[64:67], v[232:235], v[216:219], v[64:67]
	v_mfma_f32_16x16x32_bf16 v[116:119], v[228:231], v[172:175], v[116:119]
	v_mfma_f32_16x16x32_bf16 v[108:111], v[236:239], v[172:175], v[108:111]
	v_mfma_f32_16x16x32_bf16 v[100:103], v[228:231], v[180:183], v[100:103]
	v_mfma_f32_16x16x32_bf16 v[92:95], v[236:239], v[180:183], v[92:95]
	v_mfma_f32_16x16x32_bf16 v[84:87], v[228:231], v[212:215], v[84:87]
	v_mfma_f32_16x16x32_bf16 v[76:79], v[236:239], v[212:215], v[76:79]
	v_mfma_f32_16x16x32_bf16 v[68:71], v[228:231], v[220:223], v[68:71]
	v_mfma_f32_16x16x32_bf16 v[64:67], v[236:239], v[220:223], v[64:67]
	s_barrier
	s_setprio 0
	s_mov_b32 m0, s43
	v_lshl_add_u64 v[188:189], s[28:29], 0, v[128:129]
	ds_read_b128 v[164:167], v146 offset:16384
	ds_read_b128 v[172:175], v146 offset:17408
	ds_read_b128 v[176:179], v146 offset:18432
	ds_read_b128 v[180:183], v146 offset:19456
	ds_read_b128 v[208:211], v146 offset:20480
	ds_read_b128 v[212:215], v146 offset:21504
	ds_read_b128 v[216:219], v146 offset:22528
	ds_read_b128 v[220:223], v146 offset:23552
	global_load_lds_dwordx4 v[188:189], off
	v_lshl_add_u64 v[240:241], s[28:29], 0, v[134:135]
	s_mov_b32 m0, s44
	s_nop 0
	global_load_lds_dwordx4 v[240:241], off
	s_setprio 1
	s_barrier
	s_waitcnt lgkmcnt(0)
	v_mfma_f32_16x16x32_bf16 v[60:63], v[148:151], v[164:167], v[60:63]
	v_mfma_f32_16x16x32_bf16 v[56:59], v[156:159], v[164:167], v[56:59]
	v_mfma_f32_16x16x32_bf16 v[40:43], v[148:151], v[176:179], v[40:43]
	v_mfma_f32_16x16x32_bf16 v[32:35], v[156:159], v[176:179], v[32:35]
	v_mfma_f32_16x16x32_bf16 v[16:19], v[148:151], v[208:211], v[16:19]
	v_mfma_f32_16x16x32_bf16 v[12:15], v[156:159], v[208:211], v[12:15]
	v_mfma_f32_16x16x32_bf16 v[4:7], v[148:151], v[216:219], v[4:7]
	v_mfma_f32_16x16x32_bf16 v[0:3], v[156:159], v[216:219], v[0:3]
	v_mfma_f32_16x16x32_bf16 v[60:63], v[152:155], v[172:175], v[60:63]
	v_mfma_f32_16x16x32_bf16 v[56:59], v[160:163], v[172:175], v[56:59]
	v_mfma_f32_16x16x32_bf16 v[40:43], v[152:155], v[180:183], v[40:43]
	v_mfma_f32_16x16x32_bf16 v[32:35], v[160:163], v[180:183], v[32:35]
	v_mfma_f32_16x16x32_bf16 v[16:19], v[152:155], v[212:215], v[16:19]
	v_mfma_f32_16x16x32_bf16 v[12:15], v[160:163], v[212:215], v[12:15]
	v_mfma_f32_16x16x32_bf16 v[4:7], v[152:155], v[220:223], v[4:7]
	v_mfma_f32_16x16x32_bf16 v[0:3], v[160:163], v[220:223], v[0:3]
	s_barrier
	s_setprio 0
	s_add_u32 s58, s26, 0x2000
	s_addc_u32 s59, s27, 0
	s_add_i32 s57, s60, s42
	v_lshl_add_u64 v[148:149], s[58:59], 0, v[168:169]
	s_mov_b32 m0, s57
	s_nop 0
	global_load_lds_dwordx4 v[148:149], off
	v_lshl_add_u64 v[148:149], s[58:59], 0, v[132:133]
	s_add_i32 m0, s57, 0x2000
	s_nop 0
	global_load_lds_dwordx4 v[148:149], off
	s_waitcnt vmcnt(6)
	s_setprio 1
	s_barrier
	v_mfma_f32_16x16x32_bf16 v[44:47], v[224:227], v[164:167], v[44:47]
	v_mfma_f32_16x16x32_bf16 v[36:39], v[232:235], v[164:167], v[36:39]
	v_mfma_f32_16x16x32_bf16 v[20:23], v[224:227], v[176:179], v[20:23]
	v_mfma_f32_16x16x32_bf16 v[8:11], v[232:235], v[176:179], v[8:11]
	v_mfma_f32_16x16x32_bf16 v[52:55], v[224:227], v[208:211], v[52:55]
	v_mfma_f32_16x16x32_bf16 v[48:51], v[232:235], v[208:211], v[48:51]
	v_mfma_f32_16x16x32_bf16 v[28:31], v[224:227], v[216:219], v[28:31]
	v_mfma_f32_16x16x32_bf16 v[24:27], v[232:235], v[216:219], v[24:27]
	v_mfma_f32_16x16x32_bf16 v[44:47], v[228:231], v[172:175], v[44:47]
	v_mfma_f32_16x16x32_bf16 v[36:39], v[236:239], v[172:175], v[36:39]
	v_mfma_f32_16x16x32_bf16 v[20:23], v[228:231], v[180:183], v[20:23]
	v_mfma_f32_16x16x32_bf16 v[8:11], v[236:239], v[180:183], v[8:11]
	v_mfma_f32_16x16x32_bf16 v[52:55], v[228:231], v[212:215], v[52:55]
	v_mfma_f32_16x16x32_bf16 v[48:51], v[236:239], v[212:215], v[48:51]
	v_mfma_f32_16x16x32_bf16 v[28:31], v[228:231], v[220:223], v[28:31]
	v_mfma_f32_16x16x32_bf16 v[24:27], v[236:239], v[220:223], v[24:27]
	s_barrier
	s_setprio 0
	s_add_i32 s57, 0, 0x18000
	v_add_u32_e32 v147, s57, v145
	ds_read_b128 v[148:151], v147
	ds_read_b128 v[152:155], v147 offset:1024
	ds_read_b128 v[156:159], v147 offset:2048
	ds_read_b128 v[160:163], v147 offset:3072
	s_mov_b32 m0, s45
	v_lshl_add_u64 v[224:225], s[28:29], 0, v[130:131]
	ds_read_b128 v[164:167], v146 offset:32768
	ds_read_b128 v[172:175], v146 offset:33792
	ds_read_b128 v[176:179], v146 offset:34816
	ds_read_b128 v[180:183], v146 offset:35840
	ds_read_b128 v[208:211], v146 offset:36864
	ds_read_b128 v[212:215], v146 offset:37888
	ds_read_b128 v[216:219], v146 offset:38912
	ds_read_b128 v[220:223], v146 offset:39936
	global_load_lds_dwordx4 v[224:225], off
	v_lshl_add_u64 v[224:225], s[28:29], 0, v[136:137]
	s_mov_b32 m0, s46
	s_nop 0
	global_load_lds_dwordx4 v[224:225], off
	s_waitcnt lgkmcnt(8)
	s_setprio 1
	s_barrier
	s_waitcnt lgkmcnt(0)
	v_mfma_f32_16x16x32_bf16 v[124:127], v[148:151], v[164:167], v[124:127]
	v_mfma_f32_16x16x32_bf16 v[120:123], v[156:159], v[164:167], v[120:123]
	v_mfma_f32_16x16x32_bf16 v[112:115], v[148:151], v[176:179], v[112:115]
	v_mfma_f32_16x16x32_bf16 v[104:107], v[156:159], v[176:179], v[104:107]
	v_mfma_f32_16x16x32_bf16 v[96:99], v[148:151], v[208:211], v[96:99]
	v_mfma_f32_16x16x32_bf16 v[88:91], v[156:159], v[208:211], v[88:91]
	v_mfma_f32_16x16x32_bf16 v[80:83], v[148:151], v[216:219], v[80:83]
	v_mfma_f32_16x16x32_bf16 v[72:75], v[156:159], v[216:219], v[72:75]
	v_mfma_f32_16x16x32_bf16 v[124:127], v[152:155], v[172:175], v[124:127]
	v_mfma_f32_16x16x32_bf16 v[120:123], v[160:163], v[172:175], v[120:123]
	v_mfma_f32_16x16x32_bf16 v[112:115], v[152:155], v[180:183], v[112:115]
	v_mfma_f32_16x16x32_bf16 v[104:107], v[160:163], v[180:183], v[104:107]
	v_mfma_f32_16x16x32_bf16 v[96:99], v[152:155], v[212:215], v[96:99]
	v_mfma_f32_16x16x32_bf16 v[88:91], v[160:163], v[212:215], v[88:91]
	v_mfma_f32_16x16x32_bf16 v[80:83], v[152:155], v[220:223], v[80:83]
	v_mfma_f32_16x16x32_bf16 v[72:75], v[160:163], v[220:223], v[72:75]
	s_barrier
	s_setprio 0
	s_add_i32 s28, 0, 0x1c000
	s_add_i32 s29, s57, s42
	v_add_u32_e32 v147, s28, v145
	v_lshl_add_u64 v[170:171], v[170:171], 0, s[94:95]
	s_mov_b32 m0, s29
	ds_read_b128 v[224:227], v147
	ds_read_b128 v[228:231], v147 offset:1024
	ds_read_b128 v[232:235], v147 offset:2048
	ds_read_b128 v[236:239], v147 offset:3072
	global_load_lds_dwordx4 v[170:171], off
	v_lshl_add_u64 v[170:171], v[184:185], 0, s[94:95]
	s_add_i32 m0, s29, 0x2000
	s_nop 0
	global_load_lds_dwordx4 v[170:171], off
	s_setprio 1
	s_barrier
	s_waitcnt lgkmcnt(0)
	v_mfma_f32_16x16x32_bf16 v[116:119], v[224:227], v[164:167], v[116:119]
	v_mfma_f32_16x16x32_bf16 v[108:111], v[232:235], v[164:167], v[108:111]
	v_mfma_f32_16x16x32_bf16 v[100:103], v[224:227], v[176:179], v[100:103]
	v_mfma_f32_16x16x32_bf16 v[92:95], v[232:235], v[176:179], v[92:95]
	v_mfma_f32_16x16x32_bf16 v[84:87], v[224:227], v[208:211], v[84:87]
	v_mfma_f32_16x16x32_bf16 v[76:79], v[232:235], v[208:211], v[76:79]
	v_mfma_f32_16x16x32_bf16 v[68:71], v[224:227], v[216:219], v[68:71]
	v_mfma_f32_16x16x32_bf16 v[64:67], v[232:235], v[216:219], v[64:67]
	v_mfma_f32_16x16x32_bf16 v[116:119], v[228:231], v[172:175], v[116:119]
	v_mfma_f32_16x16x32_bf16 v[108:111], v[236:239], v[172:175], v[108:111]
	v_mfma_f32_16x16x32_bf16 v[100:103], v[228:231], v[180:183], v[100:103]
	v_mfma_f32_16x16x32_bf16 v[92:95], v[236:239], v[180:183], v[92:95]
	v_mfma_f32_16x16x32_bf16 v[84:87], v[228:231], v[212:215], v[84:87]
	v_mfma_f32_16x16x32_bf16 v[76:79], v[236:239], v[212:215], v[76:79]
	v_mfma_f32_16x16x32_bf16 v[68:71], v[228:231], v[220:223], v[68:71]
	v_mfma_f32_16x16x32_bf16 v[64:67], v[236:239], v[220:223], v[64:67]
	s_barrier
	s_setprio 0
	s_mov_b32 m0, s47
	v_lshl_add_u64 v[170:171], v[188:189], 0, s[94:95]
	ds_read_b128 v[164:167], v146 offset:49152
	ds_read_b128 v[172:175], v146 offset:50176
	ds_read_b128 v[176:179], v146 offset:51200
	ds_read_b128 v[180:183], v146 offset:52224
	ds_read_b128 v[208:211], v146 offset:53248
	ds_read_b128 v[212:215], v146 offset:54272
	ds_read_b128 v[216:219], v146 offset:55296
	ds_read_b128 v[220:223], v146 offset:56320
	global_load_lds_dwordx4 v[170:171], off
	v_lshl_add_u64 v[170:171], v[240:241], 0, s[94:95]
	s_mov_b32 m0, s48
	s_nop 0
	global_load_lds_dwordx4 v[170:171], off
	s_setprio 1
	s_barrier
	s_waitcnt lgkmcnt(0)
	v_mfma_f32_16x16x32_bf16 v[60:63], v[148:151], v[164:167], v[60:63]
	v_mfma_f32_16x16x32_bf16 v[56:59], v[156:159], v[164:167], v[56:59]
	v_mfma_f32_16x16x32_bf16 v[40:43], v[148:151], v[176:179], v[40:43]
	v_mfma_f32_16x16x32_bf16 v[32:35], v[156:159], v[176:179], v[32:35]
	v_mfma_f32_16x16x32_bf16 v[16:19], v[148:151], v[208:211], v[16:19]
	v_mfma_f32_16x16x32_bf16 v[12:15], v[156:159], v[208:211], v[12:15]
	v_mfma_f32_16x16x32_bf16 v[4:7], v[148:151], v[216:219], v[4:7]
	v_mfma_f32_16x16x32_bf16 v[0:3], v[156:159], v[216:219], v[0:3]
	v_mfma_f32_16x16x32_bf16 v[60:63], v[152:155], v[172:175], v[60:63]
	v_mfma_f32_16x16x32_bf16 v[56:59], v[160:163], v[172:175], v[56:59]
	v_mfma_f32_16x16x32_bf16 v[40:43], v[152:155], v[180:183], v[40:43]
	v_mfma_f32_16x16x32_bf16 v[32:35], v[160:163], v[180:183], v[32:35]
	v_mfma_f32_16x16x32_bf16 v[16:19], v[152:155], v[212:215], v[16:19]
	v_mfma_f32_16x16x32_bf16 v[12:15], v[160:163], v[212:215], v[12:15]
	v_mfma_f32_16x16x32_bf16 v[4:7], v[152:155], v[220:223], v[4:7]
	v_mfma_f32_16x16x32_bf16 v[0:3], v[160:163], v[220:223], v[0:3]
	s_barrier
	s_setprio 0
	s_add_u32 s26, s26, 0x2080
	s_addc_u32 s27, s27, 0
	s_add_i32 s28, s28, s42
	v_lshl_add_u64 v[148:149], s[26:27], 0, v[168:169]
	s_mov_b32 m0, s28
	s_nop 0
	global_load_lds_dwordx4 v[148:149], off
	v_lshl_add_u64 v[148:149], s[26:27], 0, v[132:133]
	s_add_i32 m0, s28, 0x2000
	s_nop 0
	global_load_lds_dwordx4 v[148:149], off
	s_waitcnt vmcnt(6)
	s_setprio 1
	s_barrier
	v_mfma_f32_16x16x32_bf16 v[44:47], v[224:227], v[164:167], v[44:47]
	v_mfma_f32_16x16x32_bf16 v[36:39], v[232:235], v[164:167], v[36:39]
	v_mfma_f32_16x16x32_bf16 v[20:23], v[224:227], v[176:179], v[20:23]
	v_mfma_f32_16x16x32_bf16 v[8:11], v[232:235], v[176:179], v[8:11]
	v_mfma_f32_16x16x32_bf16 v[52:55], v[224:227], v[208:211], v[52:55]
	v_mfma_f32_16x16x32_bf16 v[48:51], v[232:235], v[208:211], v[48:51]
	v_mfma_f32_16x16x32_bf16 v[28:31], v[224:227], v[216:219], v[28:31]
	v_mfma_f32_16x16x32_bf16 v[24:27], v[232:235], v[216:219], v[24:27]
	v_mfma_f32_16x16x32_bf16 v[44:47], v[228:231], v[172:175], v[44:47]
	v_mfma_f32_16x16x32_bf16 v[36:39], v[236:239], v[172:175], v[36:39]
	v_mfma_f32_16x16x32_bf16 v[20:23], v[228:231], v[180:183], v[20:23]
	v_mfma_f32_16x16x32_bf16 v[8:11], v[236:239], v[180:183], v[8:11]
	v_mfma_f32_16x16x32_bf16 v[52:55], v[228:231], v[212:215], v[52:55]
	v_mfma_f32_16x16x32_bf16 v[48:51], v[236:239], v[212:215], v[48:51]
	v_mfma_f32_16x16x32_bf16 v[28:31], v[228:231], v[220:223], v[28:31]
	v_mfma_f32_16x16x32_bf16 v[24:27], v[236:239], v[220:223], v[24:27]
	s_barrier
	s_setprio 0
	s_add_i32 s56, s56, 2
	s_add_u32 s24, s24, 0x100
	s_addc_u32 s25, s25, 0
	s_add_u32 s34, s34, 0x100
	s_addc_u32 s35, s35, 0
	s_cmp_gt_u32 s56, 5
	s_cbranch_scc0 .LBB0_1521
	s_and_b64 vcc, exec, s[6:7]
	s_cbranch_vccz .LBB0_1524
	s_barrier
